# v31
# speedup vs baseline: 1.0104x; 1.0017x over previous
.LBB2_20:
	s_add_u32 s30, s28, 0xffc80080
	s_addc_u32 s31, s29, -1
	s_cmpk_eq_i32 s58, 0xdc
	s_cselect_b32 s35, s25, s31
	s_cselect_b32 s34, s24, s30
	s_cselect_b32 s31, s27, s57
	s_cselect_b32 s30, s26, s56
	s_add_i32 m0, s37, 0xc000
	ds_read_b128 v[166:169], v143
	ds_read_b128 v[170:173], v147
	ds_read_b128 v[174:177], v149
	ds_read_b128 v[178:181], v150
	ds_read_b128 v[182:185], v151
	ds_read_b128 v[186:189], v152
	ds_read_b128 v[190:193], v153
	ds_read_b128 v[194:197], v154
	ds_read_b128 v[198:201], v155
	ds_read_b128 v[202:205], v155 offset:2048
	ds_read_b128 v[206:209], v156
	ds_read_b128 v[210:213], v156 offset:2048
	ds_read_b128 v[214:217], v155 offset:4096
	ds_read_b128 v[218:221], v155 offset:6144
	ds_read_b128 v[222:225], v156 offset:4096
	ds_read_b128 v[226:229], v156 offset:6144
	global_load_lds_dwordx4 v134, s[28:29]
	s_add_i32 m0, s37, 0xe000
	s_nop 0
	global_load_lds_dwordx4 v132, s[28:29]
	s_waitcnt vmcnt(8)
	s_waitcnt lgkmcnt(0)
	s_barrier
	v_mfma_f32_16x16x32_f16 v[124:127], v[166:169], v[198:201], v[124:127]
	v_mfma_f32_16x16x32_f16 v[124:127], v[170:173], v[206:209], v[124:127]
	v_mfma_f32_16x16x32_f16 v[120:123], v[178:181], v[206:209], v[120:123]
	v_mfma_f32_16x16x32_f16 v[120:123], v[174:177], v[198:201], v[120:123]
	v_mfma_f32_16x16x32_f16 v[112:115], v[174:177], v[202:205], v[112:115]
	v_mfma_f32_16x16x32_f16 v[112:115], v[178:181], v[210:213], v[112:115]
	v_mfma_f32_16x16x32_f16 v[116:119], v[170:173], v[210:213], v[116:119]
	v_mfma_f32_16x16x32_f16 v[116:119], v[166:169], v[202:205], v[116:119]
	v_mfma_f32_16x16x32_f16 v[108:111], v[166:169], v[214:217], v[108:111]
	v_mfma_f32_16x16x32_f16 v[108:111], v[170:173], v[222:225], v[108:111]
	v_mfma_f32_16x16x32_f16 v[100:103], v[178:181], v[222:225], v[100:103]
	v_mfma_f32_16x16x32_f16 v[100:103], v[174:177], v[214:217], v[100:103]
	v_mfma_f32_16x16x32_f16 v[84:87], v[174:177], v[218:221], v[84:87]
	v_mfma_f32_16x16x32_f16 v[84:87], v[178:181], v[226:229], v[84:87]
	v_mfma_f32_16x16x32_f16 v[92:95], v[170:173], v[226:229], v[92:95]
	v_mfma_f32_16x16x32_f16 v[92:95], v[166:169], v[218:221], v[92:95]
	v_mfma_f32_16x16x32_f16 v[104:107], v[182:185], v[198:201], v[104:107]
	v_mfma_f32_16x16x32_f16 v[104:107], v[186:189], v[206:209], v[104:107]
	v_mfma_f32_16x16x32_f16 v[96:99], v[194:197], v[206:209], v[96:99]
	v_mfma_f32_16x16x32_f16 v[96:99], v[190:193], v[198:201], v[96:99]
	v_mfma_f32_16x16x32_f16 v[80:83], v[190:193], v[202:205], v[80:83]
	v_mfma_f32_16x16x32_f16 v[80:83], v[194:197], v[210:213], v[80:83]
	v_mfma_f32_16x16x32_f16 v[88:91], v[186:189], v[210:213], v[88:91]
	v_mfma_f32_16x16x32_f16 v[88:91], v[182:185], v[202:205], v[88:91]
	v_mfma_f32_16x16x32_f16 v[76:79], v[182:185], v[214:217], v[76:79]
	v_mfma_f32_16x16x32_f16 v[76:79], v[186:189], v[222:225], v[76:79]
	v_mfma_f32_16x16x32_f16 v[72:75], v[194:197], v[222:225], v[72:75]
	v_mfma_f32_16x16x32_f16 v[72:75], v[190:193], v[214:217], v[72:75]
	v_mfma_f32_16x16x32_f16 v[64:67], v[190:193], v[218:221], v[64:67]
	v_mfma_f32_16x16x32_f16 v[64:67], v[194:197], v[226:229], v[64:67]
	v_mfma_f32_16x16x32_f16 v[68:71], v[186:189], v[226:229], v[68:71]
	v_mfma_f32_16x16x32_f16 v[68:71], v[182:185], v[218:221], v[68:71]
	s_barrier
	s_add_i32 s59, s43, s36
	s_mov_b32 m0, s59
	ds_read_b128 v[198:201], v155 offset:16384
	ds_read_b128 v[202:205], v155 offset:18432
	ds_read_b128 v[206:209], v156 offset:16384
	ds_read_b128 v[210:213], v156 offset:18432
	ds_read_b128 v[214:217], v155 offset:20480
	ds_read_b128 v[218:221], v155 offset:22528
	ds_read_b128 v[222:225], v156 offset:20480
	ds_read_b128 v[226:229], v156 offset:22528
	global_load_lds_dwordx4 v128, s[30:31]
	s_add_i32 m0, s59, 0x2000
	s_add_u32 s60, s30, 0x380000
	s_addc_u32 s61, s31, 0
	s_add_i32 s59, s44, s36
	global_load_lds_dwordx4 v130, s[30:31]
	s_mov_b32 m0, s59
	s_add_u32 s62, s30, 0x80
	s_addc_u32 s63, s31, 0
	global_load_lds_dwordx4 v128, s[60:61]
	s_add_i32 m0, s59, 0x2000
	s_add_u32 s64, s34, 0x80
	s_addc_u32 s65, s35, 0
	global_load_lds_dwordx4 v130, s[60:61]
	s_mov_b32 m0, s37
	s_nop 0
	global_load_lds_dwordx4 v128, s[34:35]
	s_mov_b32 m0, s38
	s_nop 0
	global_load_lds_dwordx4 v130, s[34:35]
	s_waitcnt vmcnt(8)
	s_waitcnt lgkmcnt(0)
	s_barrier
	v_mfma_f32_16x16x32_f16 v[60:63], v[166:169], v[198:201], v[60:63]
	v_mfma_f32_16x16x32_f16 v[60:63], v[170:173], v[206:209], v[60:63]
	v_mfma_f32_16x16x32_f16 v[56:59], v[178:181], v[206:209], v[56:59]
	v_mfma_f32_16x16x32_f16 v[56:59], v[174:177], v[198:201], v[56:59]
	v_mfma_f32_16x16x32_f16 v[48:51], v[174:177], v[202:205], v[48:51]
	v_mfma_f32_16x16x32_f16 v[48:51], v[178:181], v[210:213], v[48:51]
	v_mfma_f32_16x16x32_f16 v[52:55], v[170:173], v[210:213], v[52:55]
	v_mfma_f32_16x16x32_f16 v[52:55], v[166:169], v[202:205], v[52:55]
	v_mfma_f32_16x16x32_f16 v[40:43], v[166:169], v[214:217], v[40:43]
	v_mfma_f32_16x16x32_f16 v[40:43], v[170:173], v[222:225], v[40:43]
	v_mfma_f32_16x16x32_f16 v[32:35], v[178:181], v[222:225], v[32:35]
	v_mfma_f32_16x16x32_f16 v[32:35], v[174:177], v[214:217], v[32:35]
	v_mfma_f32_16x16x32_f16 v[8:11], v[174:177], v[218:221], v[8:11]
	v_mfma_f32_16x16x32_f16 v[8:11], v[178:181], v[226:229], v[8:11]
	v_mfma_f32_16x16x32_f16 v[12:15], v[170:173], v[226:229], v[12:15]
	v_mfma_f32_16x16x32_f16 v[12:15], v[166:169], v[218:221], v[12:15]
	v_mfma_f32_16x16x32_f16 v[44:47], v[182:185], v[198:201], v[44:47]
	v_mfma_f32_16x16x32_f16 v[44:47], v[186:189], v[206:209], v[44:47]
	v_mfma_f32_16x16x32_f16 v[36:39], v[194:197], v[206:209], v[36:39]
	v_mfma_f32_16x16x32_f16 v[36:39], v[190:193], v[198:201], v[36:39]
	v_mfma_f32_16x16x32_f16 v[24:27], v[190:193], v[202:205], v[24:27]
	v_mfma_f32_16x16x32_f16 v[24:27], v[194:197], v[210:213], v[24:27]
	v_mfma_f32_16x16x32_f16 v[28:31], v[186:189], v[210:213], v[28:31]
	v_mfma_f32_16x16x32_f16 v[28:31], v[182:185], v[202:205], v[28:31]
	v_mfma_f32_16x16x32_f16 v[20:23], v[182:185], v[214:217], v[20:23]
	v_mfma_f32_16x16x32_f16 v[20:23], v[186:189], v[222:225], v[20:23]
	v_mfma_f32_16x16x32_f16 v[16:19], v[194:197], v[222:225], v[16:19]
	v_mfma_f32_16x16x32_f16 v[16:19], v[190:193], v[214:217], v[16:19]
	v_mfma_f32_16x16x32_f16 v[0:3], v[190:193], v[218:221], v[0:3]
	v_mfma_f32_16x16x32_f16 v[0:3], v[194:197], v[226:229], v[0:3]
	v_mfma_f32_16x16x32_f16 v[4:7], v[186:189], v[226:229], v[4:7]
	v_mfma_f32_16x16x32_f16 v[4:7], v[182:185], v[218:221], v[4:7]
	s_barrier
	s_add_u32 s34, s34, 0x380000
	s_addc_u32 s35, s35, 0
	s_mov_b32 m0, s39
	ds_read_b128 v[166:169], v157
	ds_read_b128 v[170:173], v158
	ds_read_b128 v[174:177], v159
	ds_read_b128 v[178:181], v160
	ds_read_b128 v[182:185], v161
	ds_read_b128 v[186:189], v162
	ds_read_b128 v[190:193], v163
	ds_read_b128 v[194:197], v164
	ds_read_b128 v[198:201], v155 offset:32768
	ds_read_b128 v[202:205], v155 offset:34816
	ds_read_b128 v[206:209], v156 offset:32768
	ds_read_b128 v[210:213], v156 offset:34816
	ds_read_b128 v[214:217], v155 offset:36864
	ds_read_b128 v[218:221], v155 offset:38912
	ds_read_b128 v[222:225], v156 offset:36864
	ds_read_b128 v[226:229], v156 offset:38912
	global_load_lds_dwordx4 v128, s[34:35]
	s_mov_b32 m0, s40
	s_nop 0
	global_load_lds_dwordx4 v130, s[34:35]
	s_waitcnt vmcnt(8)
	s_waitcnt lgkmcnt(0)
	s_barrier
	v_mfma_f32_16x16x32_f16 v[124:127], v[166:169], v[198:201], v[124:127]
	v_mfma_f32_16x16x32_f16 v[124:127], v[170:173], v[206:209], v[124:127]
	v_mfma_f32_16x16x32_f16 v[120:123], v[178:181], v[206:209], v[120:123]
	v_mfma_f32_16x16x32_f16 v[120:123], v[174:177], v[198:201], v[120:123]
	v_mfma_f32_16x16x32_f16 v[112:115], v[174:177], v[202:205], v[112:115]
	v_mfma_f32_16x16x32_f16 v[112:115], v[178:181], v[210:213], v[112:115]
	v_mfma_f32_16x16x32_f16 v[116:119], v[170:173], v[210:213], v[116:119]
	v_mfma_f32_16x16x32_f16 v[116:119], v[166:169], v[202:205], v[116:119]
	v_mfma_f32_16x16x32_f16 v[108:111], v[166:169], v[214:217], v[108:111]
	v_mfma_f32_16x16x32_f16 v[108:111], v[170:173], v[222:225], v[108:111]
	v_mfma_f32_16x16x32_f16 v[100:103], v[178:181], v[222:225], v[100:103]
	v_mfma_f32_16x16x32_f16 v[100:103], v[174:177], v[214:217], v[100:103]
	v_mfma_f32_16x16x32_f16 v[84:87], v[174:177], v[218:221], v[84:87]
	v_mfma_f32_16x16x32_f16 v[84:87], v[178:181], v[226:229], v[84:87]
	v_mfma_f32_16x16x32_f16 v[92:95], v[170:173], v[226:229], v[92:95]
	v_mfma_f32_16x16x32_f16 v[92:95], v[166:169], v[218:221], v[92:95]
	v_mfma_f32_16x16x32_f16 v[104:107], v[182:185], v[198:201], v[104:107]
	v_mfma_f32_16x16x32_f16 v[104:107], v[186:189], v[206:209], v[104:107]
	v_mfma_f32_16x16x32_f16 v[96:99], v[194:197], v[206:209], v[96:99]
	v_mfma_f32_16x16x32_f16 v[96:99], v[190:193], v[198:201], v[96:99]
	v_mfma_f32_16x16x32_f16 v[80:83], v[190:193], v[202:205], v[80:83]
	v_mfma_f32_16x16x32_f16 v[80:83], v[194:197], v[210:213], v[80:83]
	v_mfma_f32_16x16x32_f16 v[88:91], v[186:189], v[210:213], v[88:91]
	v_mfma_f32_16x16x32_f16 v[88:91], v[182:185], v[202:205], v[88:91]
	v_mfma_f32_16x16x32_f16 v[76:79], v[182:185], v[214:217], v[76:79]
	v_mfma_f32_16x16x32_f16 v[76:79], v[186:189], v[222:225], v[76:79]
	v_mfma_f32_16x16x32_f16 v[72:75], v[194:197], v[222:225], v[72:75]
	v_mfma_f32_16x16x32_f16 v[72:75], v[190:193], v[214:217], v[72:75]
	v_mfma_f32_16x16x32_f16 v[64:67], v[190:193], v[218:221], v[64:67]
	v_mfma_f32_16x16x32_f16 v[64:67], v[194:197], v[226:229], v[64:67]
	v_mfma_f32_16x16x32_f16 v[68:71], v[186:189], v[226:229], v[68:71]
	v_mfma_f32_16x16x32_f16 v[68:71], v[182:185], v[218:221], v[68:71]
	s_barrier
	s_add_i32 s34, s46, s36
	s_mov_b32 m0, s34
	ds_read_b128 v[198:201], v155 offset:49152
	ds_read_b128 v[202:205], v155 offset:51200
	ds_read_b128 v[206:209], v156 offset:49152
	ds_read_b128 v[210:213], v156 offset:51200
	ds_read_b128 v[214:217], v155 offset:53248
	ds_read_b128 v[218:221], v155 offset:55296
	ds_read_b128 v[222:225], v156 offset:53248
	ds_read_b128 v[226:229], v156 offset:55296
	global_load_lds_dwordx4 v128, s[62:63]
	s_add_i32 m0, s34, 0x2000
	s_add_u32 s30, s30, 0x380080
	s_addc_u32 s31, s31, 0
	s_add_i32 s34, s47, s36
	global_load_lds_dwordx4 v130, s[62:63]
	s_mov_b32 m0, s34
	s_nop 0
	global_load_lds_dwordx4 v128, s[30:31]
	s_add_i32 m0, s34, 0x2000
	s_nop 0
	global_load_lds_dwordx4 v130, s[30:31]
	s_mov_b32 m0, s41
	s_nop 0
	global_load_lds_dwordx4 v128, s[64:65]
	s_mov_b32 m0, s42
	s_nop 0
	global_load_lds_dwordx4 v130, s[64:65]
	s_waitcnt vmcnt(8)
	s_waitcnt lgkmcnt(0)
	s_barrier
	v_mfma_f32_16x16x32_f16 v[60:63], v[166:169], v[198:201], v[60:63]
	v_mfma_f32_16x16x32_f16 v[60:63], v[170:173], v[206:209], v[60:63]
	v_mfma_f32_16x16x32_f16 v[56:59], v[178:181], v[206:209], v[56:59]
	v_mfma_f32_16x16x32_f16 v[56:59], v[174:177], v[198:201], v[56:59]
	v_mfma_f32_16x16x32_f16 v[48:51], v[174:177], v[202:205], v[48:51]
	v_mfma_f32_16x16x32_f16 v[48:51], v[178:181], v[210:213], v[48:51]
	v_mfma_f32_16x16x32_f16 v[52:55], v[170:173], v[210:213], v[52:55]
	v_mfma_f32_16x16x32_f16 v[52:55], v[166:169], v[202:205], v[52:55]
	v_mfma_f32_16x16x32_f16 v[40:43], v[166:169], v[214:217], v[40:43]
	v_mfma_f32_16x16x32_f16 v[40:43], v[170:173], v[222:225], v[40:43]
	v_mfma_f32_16x16x32_f16 v[32:35], v[178:181], v[222:225], v[32:35]
	v_mfma_f32_16x16x32_f16 v[32:35], v[174:177], v[214:217], v[32:35]
	v_mfma_f32_16x16x32_f16 v[8:11], v[174:177], v[218:221], v[8:11]
	v_mfma_f32_16x16x32_f16 v[8:11], v[178:181], v[226:229], v[8:11]
	v_mfma_f32_16x16x32_f16 v[12:15], v[170:173], v[226:229], v[12:15]
	v_mfma_f32_16x16x32_f16 v[12:15], v[166:169], v[218:221], v[12:15]
	v_mfma_f32_16x16x32_f16 v[44:47], v[182:185], v[198:201], v[44:47]
	v_mfma_f32_16x16x32_f16 v[44:47], v[186:189], v[206:209], v[44:47]
	v_mfma_f32_16x16x32_f16 v[36:39], v[194:197], v[206:209], v[36:39]
	v_mfma_f32_16x16x32_f16 v[36:39], v[190:193], v[198:201], v[36:39]
	v_mfma_f32_16x16x32_f16 v[24:27], v[190:193], v[202:205], v[24:27]
	v_mfma_f32_16x16x32_f16 v[24:27], v[194:197], v[210:213], v[24:27]
	v_mfma_f32_16x16x32_f16 v[28:31], v[186:189], v[210:213], v[28:31]
	v_mfma_f32_16x16x32_f16 v[28:31], v[182:185], v[202:205], v[28:31]
	v_mfma_f32_16x16x32_f16 v[20:23], v[182:185], v[214:217], v[20:23]
	v_mfma_f32_16x16x32_f16 v[20:23], v[186:189], v[222:225], v[20:23]
	v_mfma_f32_16x16x32_f16 v[16:19], v[194:197], v[222:225], v[16:19]
	v_mfma_f32_16x16x32_f16 v[16:19], v[190:193], v[214:217], v[16:19]
	v_mfma_f32_16x16x32_f16 v[0:3], v[190:193], v[218:221], v[0:3]
	v_mfma_f32_16x16x32_f16 v[0:3], v[194:197], v[226:229], v[0:3]
	v_mfma_f32_16x16x32_f16 v[4:7], v[186:189], v[226:229], v[4:7]
	v_mfma_f32_16x16x32_f16 v[4:7], v[182:185], v[218:221], v[4:7]
	s_barrier
	s_add_i32 s58, s58, 2
	s_add_u32 s56, s56, 0x100
	s_addc_u32 s57, s57, 0
	s_add_u32 s28, s28, 0x100
	s_addc_u32 s29, s29, 0
	s_cmpk_gt_u32 s58, 0xdd
	s_cbranch_scc0 .LBB2_20
	v_lshl_add_u32 v144, s55, 8, v137
	v_ashrrev_i32_e32 v145, 31, v144
	v_lshl_add_u64 v[138:139], v[144:145], 2, s[10:11]
	global_load_dword v136, v[138:139], off
	global_load_dword v140, v[138:139], off offset:64
	global_load_dword v142, v[138:139], off offset:128
	global_load_dword v146, v[138:139], off offset:192
	global_load_dword v148, v[138:139], off offset:512
	global_load_dword v174, v[138:139], off offset:576
	global_load_dword v176, v[138:139], off offset:640
	s_nop 0
	global_load_dword v138, v[138:139], off offset:704
	v_lshl_or_b32 v166, s54, 8, v141
	v_ashrrev_i32_e32 v167, 31, v166
	v_or_b32_e32 v168, 16, v144
	v_or_b32_e32 v170, 32, v144
	v_or_b32_e32 v172, 48, v144
	v_lshl_add_u64 v[166:167], v[166:167], 2, s[8:9]
	v_lshlrev_b64 v[144:145], 14, v[144:145]
	v_ashrrev_i32_e32 v169, 31, v168
	v_ashrrev_i32_e32 v171, 31, v170
	v_ashrrev_i32_e32 v173, 31, v172
	v_lshl_add_u64 v[144:145], v[166:167], 0, v[144:145]
	v_lshlrev_b64 v[168:169], 14, v[168:169]
	v_lshlrev_b64 v[170:171], 14, v[170:171]
	v_lshlrev_b64 v[172:173], 14, v[172:173]
	v_add_co_u32_e32 v178, vcc, s48, v144
	v_lshl_add_u64 v[168:169], v[166:167], 0, v[168:169]
	v_lshl_add_u64 v[170:171], v[166:167], 0, v[170:171]
	v_lshl_add_u64 v[166:167], v[166:167], 0, v[172:173]
	v_lshl_add_u64 v[172:173], v[144:145], 0, s[16:17]
	v_addc_co_u32_e32 v179, vcc, 0, v145, vcc
	s_mov_b32 s55, s45
	s_mov_b32 s54, s53
	s_mov_b64 s[28:29], s[26:27]
	s_mov_b64 s[30:31], s[24:25]
	s_waitcnt vmcnt(0)
	v_pk_mul_f32 v[126:127], v[136:137], v[126:127] op_sel_hi:[0,1]
	v_pk_mul_f32 v[124:125], v[136:137], v[124:125] op_sel_hi:[0,1]
	v_pk_mul_f32 v[122:123], v[136:137], v[122:123] op_sel_hi:[0,1]
	v_pk_mul_f32 v[120:121], v[136:137], v[120:121] op_sel_hi:[0,1]
	v_pk_mul_f32 v[46:47], v[148:149], v[46:47] op_sel_hi:[0,1]
	v_pk_mul_f32 v[44:45], v[148:149], v[44:45] op_sel_hi:[0,1]
	v_pk_mul_f32 v[106:107], v[136:137], v[106:107] op_sel_hi:[0,1]
	v_pk_mul_f32 v[104:105], v[136:137], v[104:105] op_sel_hi:[0,1]
	v_pk_mul_f32 v[98:99], v[136:137], v[98:99] op_sel_hi:[0,1]
	v_pk_mul_f32 v[96:97], v[136:137], v[96:97] op_sel_hi:[0,1]
	v_pk_mul_f32 v[118:119], v[140:141], v[118:119] op_sel_hi:[0,1]
	v_pk_mul_f32 v[116:117], v[140:141], v[116:117] op_sel_hi:[0,1]
	v_pk_mul_f32 v[114:115], v[140:141], v[114:115] op_sel_hi:[0,1]
	v_pk_mul_f32 v[112:113], v[140:141], v[112:113] op_sel_hi:[0,1]
	v_pk_mul_f32 v[90:91], v[140:141], v[90:91] op_sel_hi:[0,1]
	v_pk_mul_f32 v[88:89], v[140:141], v[88:89] op_sel_hi:[0,1]
	v_pk_mul_f32 v[82:83], v[140:141], v[82:83] op_sel_hi:[0,1]
	v_pk_mul_f32 v[80:81], v[140:141], v[80:81] op_sel_hi:[0,1]
	v_pk_mul_f32 v[110:111], v[142:143], v[110:111] op_sel_hi:[0,1]
	v_pk_mul_f32 v[108:109], v[142:143], v[108:109] op_sel_hi:[0,1]
	v_pk_mul_f32 v[102:103], v[142:143], v[102:103] op_sel_hi:[0,1]
	v_pk_mul_f32 v[100:101], v[142:143], v[100:101] op_sel_hi:[0,1]
	v_pk_mul_f32 v[78:79], v[142:143], v[78:79] op_sel_hi:[0,1]
	v_pk_mul_f32 v[76:77], v[142:143], v[76:77] op_sel_hi:[0,1]
	v_pk_mul_f32 v[74:75], v[142:143], v[74:75] op_sel_hi:[0,1]
	v_pk_mul_f32 v[72:73], v[142:143], v[72:73] op_sel_hi:[0,1]
	v_pk_mul_f32 v[94:95], v[146:147], v[94:95] op_sel_hi:[0,1]
	v_pk_mul_f32 v[92:93], v[146:147], v[92:93] op_sel_hi:[0,1]
	v_pk_mul_f32 v[86:87], v[146:147], v[86:87] op_sel_hi:[0,1]
	v_pk_mul_f32 v[84:85], v[146:147], v[84:85] op_sel_hi:[0,1]
	v_pk_mul_f32 v[70:71], v[146:147], v[70:71] op_sel_hi:[0,1]
	v_pk_mul_f32 v[68:69], v[146:147], v[68:69] op_sel_hi:[0,1]
	v_pk_mul_f32 v[66:67], v[146:147], v[66:67] op_sel_hi:[0,1]
	v_pk_mul_f32 v[64:65], v[146:147], v[64:65] op_sel_hi:[0,1]
	v_pk_mul_f32 v[62:63], v[148:149], v[62:63] op_sel_hi:[0,1]
	v_pk_mul_f32 v[60:61], v[148:149], v[60:61] op_sel_hi:[0,1]
	global_store_dwordx4 v[144:145], v[124:127], off nt
	global_store_dwordx4 v[144:145], v[120:123], off offset:64 nt
	global_store_dwordx4 v[144:145], v[104:107], off offset:512 nt
	global_store_dwordx4 v[144:145], v[96:99], off offset:576 nt
	global_store_dwordx4 v[168:169], v[116:119], off nt
	global_store_dwordx4 v[168:169], v[112:115], off offset:64 nt
	global_store_dwordx4 v[168:169], v[88:91], off offset:512 nt
	global_store_dwordx4 v[168:169], v[80:83], off offset:576 nt
	global_store_dwordx4 v[170:171], v[108:111], off nt
	global_store_dwordx4 v[170:171], v[100:103], off offset:64 nt
	global_store_dwordx4 v[170:171], v[76:79], off offset:512 nt
	global_store_dwordx4 v[170:171], v[72:75], off offset:576 nt
	global_store_dwordx4 v[166:167], v[92:95], off nt
	global_store_dwordx4 v[166:167], v[84:87], off offset:64 nt
	global_store_dwordx4 v[166:167], v[68:71], off offset:512 nt
	global_store_dwordx4 v[166:167], v[64:67], off offset:576 nt
	global_store_dwordx4 v[178:179], v[60:63], off nt
	global_store_dwordx4 v[172:173], v[44:47], off offset:512 nt
	v_pk_mul_f32 v[30:31], v[174:175], v[30:31] op_sel_hi:[0,1]
	v_pk_mul_f32 v[28:29], v[174:175], v[28:29] op_sel_hi:[0,1]
	v_add_co_u32_e32 v46, vcc, s49, v144
	v_lshl_add_u64 v[44:45], v[144:145], 0, s[18:19]
	s_nop 0
	v_addc_co_u32_e32 v47, vcc, 0, v145, vcc
	global_store_dwordx4 v[44:45], v[28:31], off offset:512 nt
	v_pk_mul_f32 v[18:19], v[176:177], v[18:19] op_sel_hi:[0,1]
	v_pk_mul_f32 v[16:17], v[176:177], v[16:17] op_sel_hi:[0,1]
	v_add_co_u32_e32 v30, vcc, s50, v144
	v_lshl_add_u64 v[28:29], v[144:145], 0, s[20:21]
	s_nop 0
	v_addc_co_u32_e32 v31, vcc, 0, v145, vcc
	v_pk_mul_f32 v[38:39], v[148:149], v[38:39] op_sel_hi:[0,1]
	v_pk_mul_f32 v[36:37], v[148:149], v[36:37] op_sel_hi:[0,1]
	v_pk_mul_f32 v[26:27], v[174:175], v[26:27] op_sel_hi:[0,1]
	v_pk_mul_f32 v[24:25], v[174:175], v[24:25] op_sel_hi:[0,1]
	global_store_dwordx4 v[28:29], v[16:19], off offset:576 nt
	global_store_dwordx4 v[172:173], v[36:39], off offset:576 nt
	global_store_dwordx4 v[44:45], v[24:27], off offset:576 nt
	v_add_co_u32_e32 v18, vcc, s51, v144
	v_pk_mul_f32 v[38:39], v[174:175], v[54:55] op_sel_hi:[0,1]
	v_pk_mul_f32 v[36:37], v[174:175], v[52:53] op_sel_hi:[0,1]
	v_pk_mul_f32 v[26:27], v[176:177], v[42:43] op_sel_hi:[0,1]
	v_pk_mul_f32 v[24:25], v[176:177], v[40:41] op_sel_hi:[0,1]
	v_addc_co_u32_e32 v19, vcc, 0, v145, vcc
	v_pk_mul_f32 v[58:59], v[148:149], v[58:59] op_sel_hi:[0,1]
	v_pk_mul_f32 v[56:57], v[148:149], v[56:57] op_sel_hi:[0,1]
	global_store_dwordx4 v[46:47], v[36:39], off nt
	global_store_dwordx4 v[30:31], v[24:27], off nt
	v_pk_mul_f32 v[22:23], v[176:177], v[22:23] op_sel_hi:[0,1]
	v_pk_mul_f32 v[38:39], v[174:175], v[50:51] op_sel_hi:[0,1]
	v_pk_mul_f32 v[36:37], v[174:175], v[48:49] op_sel_hi:[0,1]
	v_pk_mul_f32 v[26:27], v[176:177], v[34:35] op_sel_hi:[0,1]
	v_pk_mul_f32 v[24:25], v[176:177], v[32:33] op_sel_hi:[0,1]
	v_pk_mul_f32 v[20:21], v[176:177], v[20:21] op_sel_hi:[0,1]
	v_lshl_add_u64 v[16:17], v[144:145], 0, s[22:23]
	v_pk_mul_f32 v[14:15], v[138:139], v[14:15] op_sel_hi:[0,1]
	v_pk_mul_f32 v[12:13], v[138:139], v[12:13] op_sel_hi:[0,1]
	v_pk_mul_f32 v[10:11], v[138:139], v[10:11] op_sel_hi:[0,1]
	v_pk_mul_f32 v[8:9], v[138:139], v[8:9] op_sel_hi:[0,1]
	v_pk_mul_f32 v[6:7], v[138:139], v[6:7] op_sel_hi:[0,1]
	v_pk_mul_f32 v[4:5], v[138:139], v[4:5] op_sel_hi:[0,1]
	v_pk_mul_f32 v[2:3], v[138:139], v[2:3] op_sel_hi:[0,1]
	v_pk_mul_f32 v[0:1], v[138:139], v[0:1] op_sel_hi:[0,1]
	s_mov_b64 vcc, s[0:1]
	global_store_dwordx4 v[172:173], v[56:59], off offset:64 nt
	global_store_dwordx4 v[44:45], v[36:39], off offset:64 nt
	global_store_dwordx4 v[28:29], v[24:27], off offset:64 nt
	global_store_dwordx4 v[28:29], v[20:23], off offset:512 nt
	global_store_dwordx4 v[18:19], v[12:15], off nt
	global_store_dwordx4 v[16:17], v[8:11], off offset:64 nt
	global_store_dwordx4 v[16:17], v[4:7], off offset:512 nt
	global_store_dwordx4 v[16:17], v[0:3], off offset:576 nt
	s_cbranch_vccz .LBB2_8
	s_waitcnt vmcnt(0)
	s_cmpk_gt_u32 s33, 0xff
	s_cbranch_scc1 .LBB2_24
	s_barrier
